# MoE K-loops: all four even-half A-tile DMA addresses precomputed in the odd half's segment; the four LDS-DMA loads issue back to back right after the back-edge barrier
# baseline (speedup 1.0000x reference)
.LBB0_732:
	s_cmp_lg_u64 s[2:3], 0
	s_cbranch_scc1 .Lswp_guO_half
	ds_read_b64_tr_b16 v[162:163], v190 offset:32768
	ds_read_b64_tr_b16 v[164:165], v191 offset:32768
	ds_read_b64_tr_b16 v[170:171], v192 offset:32768
	ds_read_b64_tr_b16 v[172:173], v193 offset:32768
	ds_read_b128 v[214:217], v207 offset:32768
	ds_read_b128 v[224:227], v207 offset:34816
	ds_read_b128 v[232:235], v207 offset:36864
	ds_read_b128 v[240:243], v207 offset:38912
	ds_read_b64_tr_b16 v[166:167], v190 offset:40960
	ds_read_b64_tr_b16 v[168:169], v191 offset:40960
	ds_read_b64_tr_b16 v[174:175], v192 offset:40960
	ds_read_b64_tr_b16 v[176:177], v193 offset:40960
	ds_read_b128 v[218:221], v207 offset:33792
	ds_read_b128 v[228:231], v207 offset:35840
	ds_read_b128 v[236:239], v207 offset:37888
	ds_read_b128 v[244:247], v207 offset:39936
	s_lshl_b64 s[2:3], s[38:39], 18
	s_add_u32 s4, s2, 0x40000
	s_addc_u32 s5, s3, 0
	s_add_u32 s2, s67, s4
	s_addc_u32 s3, s66, s5
	s_add_u32 s4, s35, s4
	s_addc_u32 s5, s34, s5
	s_add_i32 s94, s17, 2
	s_ashr_i32 s95, s94, 31
	s_lshl_b64 s[94:95], s[94:95], 7
	s_add_u32 s94, s8, s94
	s_addc_u32 s95, s9, s95
	s_add_u32 s94, s94, 0x80
	s_addc_u32 s95, s95, 0
	v_lshl_add_u64 v[250:251], s[94:95], 0, v[178:179]
	v_lshl_add_u64 v[252:253], s[94:95], 0, v[180:181]
	v_lshl_add_u64 v[222:223], s[94:95], 0, v[182:183]
	s_setprio 1
	s_waitcnt lgkmcnt(11)
	v_mfma_f32_16x16x32_bf16 v[158:161], v[162:165], v[214:217], v[158:161]
	v_mfma_f32_16x16x32_bf16 v[154:157], v[170:173], v[214:217], v[154:157]
	ds_read_b128 v[214:217], v207 offset:49152
	s_waitcnt lgkmcnt(11)
	v_mfma_f32_16x16x32_bf16 v[146:149], v[162:165], v[224:227], v[146:149]
	v_mfma_f32_16x16x32_bf16 v[138:141], v[170:173], v[224:227], v[138:141]
	ds_read_b128 v[224:227], v207 offset:51200
	s_waitcnt lgkmcnt(11)
	v_mfma_f32_16x16x32_bf16 v[130:133], v[162:165], v[232:235], v[130:133]
	v_mfma_f32_16x16x32_bf16 v[122:125], v[170:173], v[232:235], v[122:125]
	ds_read_b128 v[232:235], v207 offset:53248
	s_waitcnt lgkmcnt(11)
	v_mfma_f32_16x16x32_bf16 v[114:117], v[162:165], v[240:243], v[114:117]
	v_mfma_f32_16x16x32_bf16 v[106:109], v[170:173], v[240:243], v[106:109]
	ds_read_b128 v[240:243], v207 offset:55296
	s_waitcnt lgkmcnt(7)
	v_mfma_f32_16x16x32_bf16 v[158:161], v[166:169], v[218:221], v[158:161]
	v_mfma_f32_16x16x32_bf16 v[154:157], v[174:177], v[218:221], v[154:157]
	ds_read_b128 v[218:221], v207 offset:50176
	s_waitcnt lgkmcnt(7)
	v_mfma_f32_16x16x32_bf16 v[146:149], v[166:169], v[228:231], v[146:149]
	v_mfma_f32_16x16x32_bf16 v[138:141], v[174:177], v[228:231], v[138:141]
	ds_read_b128 v[228:231], v207 offset:52224
	s_waitcnt lgkmcnt(7)
	v_mfma_f32_16x16x32_bf16 v[130:133], v[166:169], v[236:239], v[130:133]
	v_mfma_f32_16x16x32_bf16 v[122:125], v[174:177], v[236:239], v[122:125]
	ds_read_b128 v[236:239], v207 offset:54272
	s_waitcnt lgkmcnt(7)
	v_mfma_f32_16x16x32_bf16 v[114:117], v[166:169], v[244:247], v[114:117]
	v_mfma_f32_16x16x32_bf16 v[106:109], v[174:177], v[244:247], v[106:109]
	ds_read_b128 v[244:247], v207 offset:56320
	s_waitcnt lgkmcnt(7)
	v_mfma_f32_16x16x32_bf16 v[94:97], v[162:165], v[214:217], v[94:97]
	v_mfma_f32_16x16x32_bf16 v[86:89], v[170:173], v[214:217], v[86:89]
	ds_read_b128 v[214:217], v207 offset:32768
	s_waitcnt lgkmcnt(7)
	v_mfma_f32_16x16x32_bf16 v[78:81], v[162:165], v[224:227], v[78:81]
	v_mfma_f32_16x16x32_bf16 v[70:73], v[170:173], v[224:227], v[70:73]
	ds_read_b128 v[224:227], v207 offset:34816
	s_waitcnt lgkmcnt(7)
	v_mfma_f32_16x16x32_bf16 v[62:65], v[162:165], v[232:235], v[62:65]
	v_mfma_f32_16x16x32_bf16 v[54:57], v[170:173], v[232:235], v[54:57]
	ds_read_b128 v[232:235], v207 offset:36864
	s_waitcnt lgkmcnt(7)
	v_mfma_f32_16x16x32_bf16 v[46:49], v[162:165], v[240:243], v[46:49]
	v_mfma_f32_16x16x32_bf16 v[38:41], v[170:173], v[240:243], v[38:41]
	ds_read_b128 v[240:243], v207 offset:38912
	ds_read_b64_tr_b16 v[162:163], v190 offset:49152
	ds_read_b64_tr_b16 v[164:165], v191 offset:49152
	ds_read_b64_tr_b16 v[170:171], v192 offset:49152
	ds_read_b64_tr_b16 v[172:173], v193 offset:49152
	s_waitcnt lgkmcnt(11)
	v_mfma_f32_16x16x32_bf16 v[94:97], v[166:169], v[218:221], v[94:97]
	v_mfma_f32_16x16x32_bf16 v[86:89], v[174:177], v[218:221], v[86:89]
	ds_read_b128 v[218:221], v207 offset:33792
	s_waitcnt lgkmcnt(11)
	v_mfma_f32_16x16x32_bf16 v[78:81], v[166:169], v[228:231], v[78:81]
	v_mfma_f32_16x16x32_bf16 v[70:73], v[174:177], v[228:231], v[70:73]
	ds_read_b128 v[228:231], v207 offset:35840
	s_waitcnt lgkmcnt(11)
	v_mfma_f32_16x16x32_bf16 v[62:65], v[166:169], v[236:239], v[62:65]
	v_mfma_f32_16x16x32_bf16 v[54:57], v[174:177], v[236:239], v[54:57]
	ds_read_b128 v[236:239], v207 offset:37888
	s_waitcnt lgkmcnt(11)
	v_mfma_f32_16x16x32_bf16 v[46:49], v[166:169], v[244:247], v[46:49]
	v_mfma_f32_16x16x32_bf16 v[38:41], v[174:177], v[244:247], v[38:41]
	ds_read_b128 v[244:247], v207 offset:39936
	ds_read_b64_tr_b16 v[166:167], v190 offset:57344
	ds_read_b64_tr_b16 v[168:169], v191 offset:57344
	ds_read_b64_tr_b16 v[174:175], v192 offset:57344
	ds_read_b64_tr_b16 v[176:177], v193 offset:57344
	s_waitcnt lgkmcnt(8)
	v_mfma_f32_16x16x32_bf16 v[150:153], v[162:165], v[214:217], v[150:153]
	v_mfma_f32_16x16x32_bf16 v[142:145], v[170:173], v[214:217], v[142:145]
	ds_read_b128 v[214:217], v207 offset:49152
	v_mfma_f32_16x16x32_bf16 v[134:137], v[162:165], v[224:227], v[134:137]
	v_mfma_f32_16x16x32_bf16 v[126:129], v[170:173], v[224:227], v[126:129]
	ds_read_b128 v[224:227], v207 offset:51200
	v_mfma_f32_16x16x32_bf16 v[118:121], v[162:165], v[232:235], v[118:121]
	v_mfma_f32_16x16x32_bf16 v[110:113], v[170:173], v[232:235], v[110:113]
	ds_read_b128 v[232:235], v207 offset:53248
	v_mfma_f32_16x16x32_bf16 v[102:105], v[162:165], v[240:243], v[102:105]
	v_mfma_f32_16x16x32_bf16 v[98:101], v[170:173], v[240:243], v[98:101]
	ds_read_b128 v[240:243], v207 offset:55296
	s_waitcnt lgkmcnt(4)
	v_mfma_f32_16x16x32_bf16 v[150:153], v[166:169], v[218:221], v[150:153]
	v_mfma_f32_16x16x32_bf16 v[142:145], v[174:177], v[218:221], v[142:145]
	ds_read_b128 v[218:221], v207 offset:50176
	v_mfma_f32_16x16x32_bf16 v[134:137], v[166:169], v[228:231], v[134:137]
	v_mfma_f32_16x16x32_bf16 v[126:129], v[174:177], v[228:231], v[126:129]
	ds_read_b128 v[228:231], v207 offset:52224
	v_mfma_f32_16x16x32_bf16 v[118:121], v[166:169], v[236:239], v[118:121]
	v_mfma_f32_16x16x32_bf16 v[110:113], v[174:177], v[236:239], v[110:113]
	ds_read_b128 v[236:239], v207 offset:54272
	v_mfma_f32_16x16x32_bf16 v[102:105], v[166:169], v[244:247], v[102:105]
	v_mfma_f32_16x16x32_bf16 v[98:101], v[174:177], v[244:247], v[98:101]
	ds_read_b128 v[244:247], v207 offset:56320
	s_waitcnt lgkmcnt(7)
	v_mfma_f32_16x16x32_bf16 v[90:93], v[162:165], v[214:217], v[90:93]
	v_mfma_f32_16x16x32_bf16 v[82:85], v[170:173], v[214:217], v[82:85]
	s_waitcnt vmcnt(9)
	v_cvt_pk_bf16_f32 v248, v2, v3
	v_cvt_pk_bf16_f32 v249, v4, v5
	ds_write_b64 v197, v[248:249] offset:16384
	global_load_dwordx4 v[2:5], v189, s[2:3]
	s_waitcnt lgkmcnt(7)
	v_mfma_f32_16x16x32_bf16 v[74:77], v[162:165], v[224:227], v[74:77]
	v_mfma_f32_16x16x32_bf16 v[66:69], v[170:173], v[224:227], v[66:69]
	s_waitcnt vmcnt(9)
	v_cvt_pk_bf16_f32 v248, v6, v7
	v_cvt_pk_bf16_f32 v249, v8, v9
	ds_write_b64 v196, v[248:249] offset:16384
	global_load_dwordx4 v[6:9], v189, s[4:5]
	s_waitcnt lgkmcnt(7)
	v_mfma_f32_16x16x32_bf16 v[58:61], v[162:165], v[232:235], v[58:61]
	v_mfma_f32_16x16x32_bf16 v[50:53], v[170:173], v[232:235], v[50:53]
	s_waitcnt vmcnt(9)
	v_cvt_pk_bf16_f32 v248, v10, v11
	v_cvt_pk_bf16_f32 v249, v12, v13
	ds_write_b64 v197, v[248:249]
	s_add_u32 s98, s2, 0x2000
	s_addc_u32 s99, s3, 0
	global_load_dwordx4 v[10:13], v189, s[98:99]
	s_waitcnt lgkmcnt(7)
	v_mfma_f32_16x16x32_bf16 v[42:45], v[162:165], v[240:243], v[42:45]
	v_mfma_f32_16x16x32_bf16 v[30:33], v[170:173], v[240:243], v[30:33]
	s_waitcnt vmcnt(9)
	v_cvt_pk_bf16_f32 v248, v14, v15
	v_cvt_pk_bf16_f32 v249, v16, v17
	ds_write_b64 v195, v[248:249] offset:16384
	s_add_u32 s100, s4, 0x2000
	s_addc_u32 s101, s5, 0
	global_load_dwordx4 v[14:17], v189, s[100:101]
	s_waitcnt lgkmcnt(7)
	v_mfma_f32_16x16x32_bf16 v[90:93], v[166:169], v[218:221], v[90:93]
	v_mfma_f32_16x16x32_bf16 v[82:85], v[174:177], v[218:221], v[82:85]
	s_waitcnt vmcnt(9)
	v_cvt_pk_bf16_f32 v248, v18, v19
	v_cvt_pk_bf16_f32 v249, v20, v21
	ds_write_b64 v196, v[248:249]
	s_add_u32 s98, s2, 0x4000
	s_addc_u32 s99, s3, 0
	global_load_dwordx4 v[18:21], v189, s[98:99]
	s_waitcnt lgkmcnt(7)
	v_mfma_f32_16x16x32_bf16 v[74:77], v[166:169], v[228:231], v[74:77]
	v_mfma_f32_16x16x32_bf16 v[66:69], v[174:177], v[228:231], v[66:69]
	s_waitcnt vmcnt(9)
	v_cvt_pk_bf16_f32 v248, v22, v23
	v_cvt_pk_bf16_f32 v249, v24, v25
	ds_write_b64 v194, v[248:249] offset:16384
	s_add_u32 s100, s4, 0x4000
	s_addc_u32 s101, s5, 0
	global_load_dwordx4 v[22:25], v189, s[100:101]
	s_waitcnt lgkmcnt(7)
	v_mfma_f32_16x16x32_bf16 v[58:61], v[166:169], v[236:239], v[58:61]
	v_mfma_f32_16x16x32_bf16 v[50:53], v[174:177], v[236:239], v[50:53]
	s_waitcnt vmcnt(9)
	v_cvt_pk_bf16_f32 v248, v26, v27
	v_cvt_pk_bf16_f32 v249, v28, v29
	ds_write_b64 v195, v[248:249]
	s_add_u32 s98, s2, 0x6000
	s_addc_u32 s99, s3, 0
	global_load_dwordx4 v[26:29], v189, s[98:99]
	s_waitcnt lgkmcnt(7)
	v_mfma_f32_16x16x32_bf16 v[42:45], v[166:169], v[244:247], v[42:45]
	v_mfma_f32_16x16x32_bf16 v[30:33], v[174:177], v[244:247], v[30:33]
	s_waitcnt vmcnt(9)
	v_cvt_pk_bf16_f32 v248, v34, v35
	v_cvt_pk_bf16_f32 v249, v36, v37
	ds_write_b64 v194, v[248:249]
	s_add_u32 s100, s4, 0x6000
	s_addc_u32 s101, s5, 0
	global_load_dwordx4 v[34:37], v189, s[100:101]
	v_lshl_add_u64 v[248:249], s[94:95], 0, v[184:185]
	s_setprio 0
.LBB0_736:
.Lswp_guO_tail:
	s_add_i32 m0, s51, 0x8000
	s_waitcnt vmcnt(8)
	s_waitcnt lgkmcnt(0)
	s_barrier
	s_cmp_gt_u32 s17, 29
	s_cbranch_scc1 .LBB0_738
	global_load_lds_dwordx4 v[250:251], off
	s_add_i32 m0, s51, 0xa000
	s_mov_b32 s34, s17
	global_load_lds_dwordx4 v[252:253], off
	s_andn2_b64 vcc, exec, s[0:1]
	s_add_i32 m0, s51, 0xc000
	s_cbranch_vccnz .Lrot_gu_two
	global_load_lds_dwordx4 v[222:223], off
	s_add_i32 m0, s51, 0xe000
	s_nop 0
	global_load_lds_dwordx4 v[248:249], off
.Lrot_gu_two:
	s_add_i32 s17, s34, 2
	s_mov_b32 s4, s17
	s_ashr_i32 s5, s4, 31
	s_mov_b64 s[38:39], s[94:95]
	v_cndmask_b32_e64 v162, 0, 1, s[0:1]
	v_cmp_ne_u32_e64 s[2:3], 1, v162
	s_branch .LBB0_726

.Lswp_guO_half:
	ds_read_b64_tr_b16 v[162:163], v190 offset:32768
	ds_read_b64_tr_b16 v[164:165], v191 offset:32768
	ds_read_b64_tr_b16 v[170:171], v192 offset:32768
	ds_read_b64_tr_b16 v[172:173], v193 offset:32768
	ds_read_b128 v[214:217], v207 offset:32768
	ds_read_b128 v[224:227], v207 offset:34816
	ds_read_b128 v[232:235], v207 offset:36864
	ds_read_b128 v[240:243], v207 offset:38912
	ds_read_b64_tr_b16 v[166:167], v190 offset:40960
	ds_read_b64_tr_b16 v[168:169], v191 offset:40960
	ds_read_b64_tr_b16 v[174:175], v192 offset:40960
	ds_read_b64_tr_b16 v[176:177], v193 offset:40960
	ds_read_b128 v[218:221], v207 offset:33792
	ds_read_b128 v[228:231], v207 offset:35840
	ds_read_b128 v[236:239], v207 offset:37888
	ds_read_b128 v[244:247], v207 offset:39936
	s_lshl_b64 s[2:3], s[38:39], 18
	s_add_u32 s4, s2, 0x40000
	s_addc_u32 s5, s3, 0
	s_add_u32 s2, s67, s4
	s_addc_u32 s3, s66, s5
	s_add_u32 s4, s35, s4
	s_addc_u32 s5, s34, s5
	s_add_i32 s94, s17, 2
	s_ashr_i32 s95, s94, 31
	s_lshl_b64 s[94:95], s[94:95], 7
	s_add_u32 s94, s8, s94
	s_addc_u32 s95, s9, s95
	s_add_u32 s94, s94, 0x80
	s_addc_u32 s95, s95, 0
	v_lshl_add_u64 v[250:251], s[94:95], 0, v[178:179]
	v_lshl_add_u64 v[252:253], s[94:95], 0, v[180:181]
	v_lshl_add_u64 v[222:223], s[94:95], 0, v[182:183]
	s_setprio 1
	s_waitcnt lgkmcnt(11)
	v_mfma_f32_16x16x32_bf16 v[158:161], v[162:165], v[214:217], v[158:161]
	v_mfma_f32_16x16x32_bf16 v[154:157], v[170:173], v[214:217], v[154:157]
	ds_read_b128 v[214:217], v207 offset:32768
	s_waitcnt lgkmcnt(11)
	v_mfma_f32_16x16x32_bf16 v[146:149], v[162:165], v[224:227], v[146:149]
	v_mfma_f32_16x16x32_bf16 v[138:141], v[170:173], v[224:227], v[138:141]
	ds_read_b128 v[224:227], v207 offset:34816
	s_waitcnt lgkmcnt(11)
	v_mfma_f32_16x16x32_bf16 v[130:133], v[162:165], v[232:235], v[130:133]
	v_mfma_f32_16x16x32_bf16 v[122:125], v[170:173], v[232:235], v[122:125]
	ds_read_b128 v[232:235], v207 offset:36864
	s_waitcnt lgkmcnt(11)
	v_mfma_f32_16x16x32_bf16 v[114:117], v[162:165], v[240:243], v[114:117]
	v_mfma_f32_16x16x32_bf16 v[106:109], v[170:173], v[240:243], v[106:109]
	ds_read_b128 v[240:243], v207 offset:38912
	ds_read_b64_tr_b16 v[162:163], v190 offset:49152
	ds_read_b64_tr_b16 v[164:165], v191 offset:49152
	ds_read_b64_tr_b16 v[170:171], v192 offset:49152
	ds_read_b64_tr_b16 v[172:173], v193 offset:49152
	s_waitcnt lgkmcnt(11)
	v_mfma_f32_16x16x32_bf16 v[158:161], v[166:169], v[218:221], v[158:161]
	v_mfma_f32_16x16x32_bf16 v[154:157], v[174:177], v[218:221], v[154:157]
	ds_read_b128 v[218:221], v207 offset:33792
	s_waitcnt lgkmcnt(11)
	v_mfma_f32_16x16x32_bf16 v[146:149], v[166:169], v[228:231], v[146:149]
	v_mfma_f32_16x16x32_bf16 v[138:141], v[174:177], v[228:231], v[138:141]
	ds_read_b128 v[228:231], v207 offset:35840
	s_waitcnt lgkmcnt(11)
	v_mfma_f32_16x16x32_bf16 v[130:133], v[166:169], v[236:239], v[130:133]
	v_mfma_f32_16x16x32_bf16 v[122:125], v[174:177], v[236:239], v[122:125]
	ds_read_b128 v[236:239], v207 offset:37888
	s_waitcnt lgkmcnt(11)
	v_mfma_f32_16x16x32_bf16 v[114:117], v[166:169], v[244:247], v[114:117]
	v_mfma_f32_16x16x32_bf16 v[106:109], v[174:177], v[244:247], v[106:109]
	ds_read_b128 v[244:247], v207 offset:39936
	ds_read_b64_tr_b16 v[166:167], v190 offset:57344
	ds_read_b64_tr_b16 v[168:169], v191 offset:57344
	ds_read_b64_tr_b16 v[174:175], v192 offset:57344
	ds_read_b64_tr_b16 v[176:177], v193 offset:57344
	s_waitcnt lgkmcnt(8)
	v_mfma_f32_16x16x32_bf16 v[150:153], v[162:165], v[214:217], v[150:153]
	v_mfma_f32_16x16x32_bf16 v[142:145], v[170:173], v[214:217], v[142:145]
	s_waitcnt vmcnt(9)
	v_cvt_pk_bf16_f32 v248, v2, v3
	v_cvt_pk_bf16_f32 v249, v4, v5
	ds_write_b64 v197, v[248:249] offset:16384
	global_load_dwordx4 v[2:5], v189, s[2:3]
	v_mfma_f32_16x16x32_bf16 v[134:137], v[162:165], v[224:227], v[134:137]
	v_mfma_f32_16x16x32_bf16 v[126:129], v[170:173], v[224:227], v[126:129]
	s_waitcnt vmcnt(9)
	v_cvt_pk_bf16_f32 v248, v6, v7
	v_cvt_pk_bf16_f32 v249, v8, v9
	ds_write_b64 v196, v[248:249] offset:16384
	global_load_dwordx4 v[6:9], v189, s[4:5]
	v_mfma_f32_16x16x32_bf16 v[118:121], v[162:165], v[232:235], v[118:121]
	v_mfma_f32_16x16x32_bf16 v[110:113], v[170:173], v[232:235], v[110:113]
	s_waitcnt vmcnt(9)
	v_cvt_pk_bf16_f32 v248, v10, v11
	v_cvt_pk_bf16_f32 v249, v12, v13
	ds_write_b64 v197, v[248:249]
	s_add_u32 s98, s2, 0x2000
	s_addc_u32 s99, s3, 0
	global_load_dwordx4 v[10:13], v189, s[98:99]
	v_mfma_f32_16x16x32_bf16 v[102:105], v[162:165], v[240:243], v[102:105]
	v_mfma_f32_16x16x32_bf16 v[98:101], v[170:173], v[240:243], v[98:101]
	s_waitcnt vmcnt(9)
	v_cvt_pk_bf16_f32 v248, v14, v15
	v_cvt_pk_bf16_f32 v249, v16, v17
	ds_write_b64 v195, v[248:249] offset:16384
	s_add_u32 s100, s4, 0x2000
	s_addc_u32 s101, s5, 0
	global_load_dwordx4 v[14:17], v189, s[100:101]
	s_waitcnt lgkmcnt(4)
	v_mfma_f32_16x16x32_bf16 v[150:153], v[166:169], v[218:221], v[150:153]
	v_mfma_f32_16x16x32_bf16 v[142:145], v[174:177], v[218:221], v[142:145]
	s_waitcnt vmcnt(9)
	v_cvt_pk_bf16_f32 v248, v18, v19
	v_cvt_pk_bf16_f32 v249, v20, v21
	ds_write_b64 v196, v[248:249]
	s_add_u32 s98, s2, 0x4000
	s_addc_u32 s99, s3, 0
	global_load_dwordx4 v[18:21], v189, s[98:99]
	v_mfma_f32_16x16x32_bf16 v[134:137], v[166:169], v[228:231], v[134:137]
	v_mfma_f32_16x16x32_bf16 v[126:129], v[174:177], v[228:231], v[126:129]
	s_waitcnt vmcnt(9)
	v_cvt_pk_bf16_f32 v248, v22, v23
	v_cvt_pk_bf16_f32 v249, v24, v25
	ds_write_b64 v194, v[248:249] offset:16384
	s_add_u32 s100, s4, 0x4000
	s_addc_u32 s101, s5, 0
	global_load_dwordx4 v[22:25], v189, s[100:101]
	v_mfma_f32_16x16x32_bf16 v[118:121], v[166:169], v[236:239], v[118:121]
	v_mfma_f32_16x16x32_bf16 v[110:113], v[174:177], v[236:239], v[110:113]
	s_waitcnt vmcnt(9)
	v_cvt_pk_bf16_f32 v248, v26, v27
	v_cvt_pk_bf16_f32 v249, v28, v29
	ds_write_b64 v195, v[248:249]
	s_add_u32 s98, s2, 0x6000
	s_addc_u32 s99, s3, 0
	global_load_dwordx4 v[26:29], v189, s[98:99]
	v_mfma_f32_16x16x32_bf16 v[102:105], v[166:169], v[244:247], v[102:105]
	v_mfma_f32_16x16x32_bf16 v[98:101], v[174:177], v[244:247], v[98:101]
	s_waitcnt vmcnt(9)
	v_cvt_pk_bf16_f32 v248, v34, v35
	v_cvt_pk_bf16_f32 v249, v36, v37
	ds_write_b64 v194, v[248:249]
	s_add_u32 s100, s4, 0x6000
	s_addc_u32 s101, s5, 0
	global_load_dwordx4 v[34:37], v189, s[100:101]
	v_lshl_add_u64 v[248:249], s[94:95], 0, v[184:185]
	s_setprio 0
	s_branch .Lswp_guO_tail

.LBB0_864:
	s_cmp_lg_u64 s[2:3], 0
	s_cbranch_scc1 .Lswp_dnO_half
	ds_read_b64_tr_b16 v[164:165], v190 offset:32768
	ds_read_b64_tr_b16 v[166:167], v191 offset:32768
	ds_read_b64_tr_b16 v[172:173], v192 offset:32768
	ds_read_b64_tr_b16 v[174:175], v193 offset:32768
	ds_read_b128 v[210:213], v207 offset:32768
	ds_read_b128 v[218:221], v207 offset:34816
	ds_read_b128 v[228:231], v207 offset:36864
	ds_read_b128 v[236:239], v207 offset:38912
	ds_read_b64_tr_b16 v[168:169], v190 offset:40960
	ds_read_b64_tr_b16 v[170:171], v191 offset:40960
	ds_read_b64_tr_b16 v[176:177], v192 offset:40960
	ds_read_b64_tr_b16 v[178:179], v193 offset:40960
	ds_read_b128 v[214:217], v207 offset:33792
	ds_read_b128 v[224:227], v207 offset:35840
	ds_read_b128 v[232:235], v207 offset:37888
	ds_read_b128 v[240:243], v207 offset:39936
	s_lshl_b64 s[2:3], s[48:49], 19
	s_add_u32 s48, s2, 0x80000
	s_addc_u32 s49, s3, 0
	s_add_u32 s2, s74, s48
	s_addc_u32 s3, s43, s49
	s_add_u32 s48, s37, s48
	s_addc_u32 s49, s35, s49
	s_add_i32 s94, s34, 2
	s_ashr_i32 s95, s94, 31
	s_lshl_b64 s[94:95], s[94:95], 7
	s_add_u32 s94, s22, s94
	s_addc_u32 s95, s23, s95
	s_add_u32 s94, s94, 0x80
	s_addc_u32 s95, s95, 0
	v_lshl_add_u64 v[250:251], s[94:95], 0, v[180:181]
	v_lshl_add_u64 v[252:253], s[94:95], 0, v[182:183]
	v_lshl_add_u64 v[222:223], s[94:95], 0, v[184:185]
	v_lshl_add_u64 v[246:247], s[94:95], 0, v[186:187]
	s_setprio 1
	s_waitcnt lgkmcnt(11)
	v_mfma_f32_16x16x32_bf16 v[160:163], v[164:167], v[210:213], v[160:163]
	v_mfma_f32_16x16x32_bf16 v[156:159], v[172:175], v[210:213], v[156:159]
	ds_read_b128 v[210:213], v207 offset:49152
	s_waitcnt lgkmcnt(11)
	v_mfma_f32_16x16x32_bf16 v[152:155], v[164:167], v[218:221], v[152:155]
	v_mfma_f32_16x16x32_bf16 v[148:151], v[172:175], v[218:221], v[148:151]
	ds_read_b128 v[218:221], v207 offset:51200
	s_waitcnt lgkmcnt(11)
	v_mfma_f32_16x16x32_bf16 v[136:139], v[164:167], v[228:231], v[136:139]
	v_mfma_f32_16x16x32_bf16 v[132:135], v[172:175], v[228:231], v[132:135]
	ds_read_b128 v[228:231], v207 offset:53248
	s_waitcnt lgkmcnt(11)
	v_mfma_f32_16x16x32_bf16 v[120:123], v[164:167], v[236:239], v[120:123]
	v_mfma_f32_16x16x32_bf16 v[116:119], v[172:175], v[236:239], v[116:119]
	ds_read_b128 v[236:239], v207 offset:55296
	s_waitcnt lgkmcnt(7)
	v_mfma_f32_16x16x32_bf16 v[160:163], v[168:171], v[214:217], v[160:163]
	v_mfma_f32_16x16x32_bf16 v[156:159], v[176:179], v[214:217], v[156:159]
	ds_read_b128 v[214:217], v207 offset:50176
	s_waitcnt lgkmcnt(7)
	v_mfma_f32_16x16x32_bf16 v[152:155], v[168:171], v[224:227], v[152:155]
	v_mfma_f32_16x16x32_bf16 v[148:151], v[176:179], v[224:227], v[148:151]
	ds_read_b128 v[224:227], v207 offset:52224
	s_waitcnt lgkmcnt(7)
	v_mfma_f32_16x16x32_bf16 v[136:139], v[168:171], v[232:235], v[136:139]
	v_mfma_f32_16x16x32_bf16 v[132:135], v[176:179], v[232:235], v[132:135]
	ds_read_b128 v[232:235], v207 offset:54272
	s_waitcnt lgkmcnt(7)
	v_mfma_f32_16x16x32_bf16 v[120:123], v[168:171], v[240:243], v[120:123]
	v_mfma_f32_16x16x32_bf16 v[116:119], v[176:179], v[240:243], v[116:119]
	ds_read_b128 v[240:243], v207 offset:56320
	s_waitcnt lgkmcnt(7)
	v_mfma_f32_16x16x32_bf16 v[80:83], v[164:167], v[210:213], v[80:83]
	v_mfma_f32_16x16x32_bf16 v[68:71], v[172:175], v[210:213], v[68:71]
	ds_read_b128 v[210:213], v207 offset:32768
	s_waitcnt lgkmcnt(7)
	v_mfma_f32_16x16x32_bf16 v[48:51], v[164:167], v[218:221], v[48:51]
	v_mfma_f32_16x16x32_bf16 v[44:47], v[172:175], v[218:221], v[44:47]
	ds_read_b128 v[218:221], v207 offset:34816
	s_waitcnt lgkmcnt(7)
	v_mfma_f32_16x16x32_bf16 v[32:35], v[164:167], v[228:231], v[32:35]
	v_mfma_f32_16x16x32_bf16 v[28:31], v[172:175], v[228:231], v[28:31]
	ds_read_b128 v[228:231], v207 offset:36864
	s_waitcnt lgkmcnt(7)
	v_mfma_f32_16x16x32_bf16 v[16:19], v[164:167], v[236:239], v[16:19]
	v_mfma_f32_16x16x32_bf16 v[12:15], v[172:175], v[236:239], v[12:15]
	ds_read_b128 v[236:239], v207 offset:38912
	ds_read_b64_tr_b16 v[164:165], v190 offset:49152
	ds_read_b64_tr_b16 v[166:167], v191 offset:49152
	ds_read_b64_tr_b16 v[172:173], v192 offset:49152
	ds_read_b64_tr_b16 v[174:175], v193 offset:49152
	s_waitcnt lgkmcnt(11)
	v_mfma_f32_16x16x32_bf16 v[80:83], v[168:171], v[214:217], v[80:83]
	v_mfma_f32_16x16x32_bf16 v[68:71], v[176:179], v[214:217], v[68:71]
	ds_read_b128 v[214:217], v207 offset:33792
	s_waitcnt lgkmcnt(11)
	v_mfma_f32_16x16x32_bf16 v[48:51], v[168:171], v[224:227], v[48:51]
	v_mfma_f32_16x16x32_bf16 v[44:47], v[176:179], v[224:227], v[44:47]
	ds_read_b128 v[224:227], v207 offset:35840
	s_waitcnt lgkmcnt(11)
	v_mfma_f32_16x16x32_bf16 v[32:35], v[168:171], v[232:235], v[32:35]
	v_mfma_f32_16x16x32_bf16 v[28:31], v[176:179], v[232:235], v[28:31]
	ds_read_b128 v[232:235], v207 offset:37888
	s_waitcnt lgkmcnt(11)
	v_mfma_f32_16x16x32_bf16 v[16:19], v[168:171], v[240:243], v[16:19]
	v_mfma_f32_16x16x32_bf16 v[12:15], v[176:179], v[240:243], v[12:15]
	ds_read_b128 v[240:243], v207 offset:39936
	ds_read_b64_tr_b16 v[168:169], v190 offset:57344
	ds_read_b64_tr_b16 v[170:171], v191 offset:57344
	ds_read_b64_tr_b16 v[176:177], v192 offset:57344
	ds_read_b64_tr_b16 v[178:179], v193 offset:57344
	s_waitcnt lgkmcnt(8)
	v_mfma_f32_16x16x32_bf16 v[144:147], v[164:167], v[210:213], v[144:147]
	v_mfma_f32_16x16x32_bf16 v[140:143], v[172:175], v[210:213], v[140:143]
	ds_read_b128 v[210:213], v207 offset:49152
	v_mfma_f32_16x16x32_bf16 v[128:131], v[164:167], v[218:221], v[128:131]
	v_mfma_f32_16x16x32_bf16 v[124:127], v[172:175], v[218:221], v[124:127]
	ds_read_b128 v[218:221], v207 offset:51200
	v_mfma_f32_16x16x32_bf16 v[112:115], v[164:167], v[228:231], v[112:115]
	v_mfma_f32_16x16x32_bf16 v[108:111], v[172:175], v[228:231], v[108:111]
	ds_read_b128 v[228:231], v207 offset:53248
	v_mfma_f32_16x16x32_bf16 v[104:107], v[164:167], v[236:239], v[104:107]
	v_mfma_f32_16x16x32_bf16 v[100:103], v[172:175], v[236:239], v[100:103]
	ds_read_b128 v[236:239], v207 offset:55296
	s_waitcnt lgkmcnt(4)
	v_mfma_f32_16x16x32_bf16 v[144:147], v[168:171], v[214:217], v[144:147]
	v_mfma_f32_16x16x32_bf16 v[140:143], v[176:179], v[214:217], v[140:143]
	ds_read_b128 v[214:217], v207 offset:50176
	v_mfma_f32_16x16x32_bf16 v[128:131], v[168:171], v[224:227], v[128:131]
	v_mfma_f32_16x16x32_bf16 v[124:127], v[176:179], v[224:227], v[124:127]
	ds_read_b128 v[224:227], v207 offset:52224
	v_mfma_f32_16x16x32_bf16 v[112:115], v[168:171], v[232:235], v[112:115]
	v_mfma_f32_16x16x32_bf16 v[108:111], v[176:179], v[232:235], v[108:111]
	ds_read_b128 v[232:235], v207 offset:54272
	v_mfma_f32_16x16x32_bf16 v[104:107], v[168:171], v[240:243], v[104:107]
	v_mfma_f32_16x16x32_bf16 v[100:103], v[176:179], v[240:243], v[100:103]
	ds_read_b128 v[240:243], v207 offset:56320
	s_waitcnt lgkmcnt(7)
	v_mfma_f32_16x16x32_bf16 v[56:59], v[164:167], v[210:213], v[56:59]
	v_mfma_f32_16x16x32_bf16 v[52:55], v[172:175], v[210:213], v[52:55]
	s_waitcnt vmcnt(9)
	v_cvt_pk_bf16_f32 v244, v64, v65
	v_cvt_pk_bf16_f32 v245, v66, v67
	ds_write_b64 v196, v[244:245] offset:16384
	global_load_dwordx4 v[64:67], v189, s[2:3]
	s_waitcnt lgkmcnt(7)
	v_mfma_f32_16x16x32_bf16 v[40:43], v[164:167], v[218:221], v[40:43]
	v_mfma_f32_16x16x32_bf16 v[36:39], v[172:175], v[218:221], v[36:39]
	s_waitcnt vmcnt(9)
	v_cvt_pk_bf16_f32 v244, v60, v61
	v_cvt_pk_bf16_f32 v245, v62, v63
	ds_write_b64 v197, v[244:245] offset:16384
	global_load_dwordx4 v[60:63], v189, s[48:49]
	s_waitcnt lgkmcnt(7)
	v_mfma_f32_16x16x32_bf16 v[24:27], v[164:167], v[228:231], v[24:27]
	v_mfma_f32_16x16x32_bf16 v[20:23], v[172:175], v[228:231], v[20:23]
	s_waitcnt vmcnt(9)
	v_cvt_pk_bf16_f32 v244, v76, v77
	v_cvt_pk_bf16_f32 v245, v78, v79
	ds_write_b64 v195, v[244:245] offset:16384
	s_add_u32 s98, s2, 0x4000
	s_addc_u32 s99, s3, 0
	global_load_dwordx4 v[76:79], v189, s[98:99]
	s_waitcnt lgkmcnt(7)
	v_mfma_f32_16x16x32_bf16 v[8:11], v[164:167], v[236:239], v[8:11]
	v_mfma_f32_16x16x32_bf16 v[2:5], v[172:175], v[236:239], v[4:7]
	s_waitcnt vmcnt(9)
	v_cvt_pk_bf16_f32 v244, v72, v73
	v_cvt_pk_bf16_f32 v245, v74, v75
	ds_write_b64 v197, v[244:245]
	s_add_u32 s100, s48, 0x4000
	s_addc_u32 s101, s49, 0
	global_load_dwordx4 v[72:75], v189, s[100:101]
	s_waitcnt lgkmcnt(7)
	v_mfma_f32_16x16x32_bf16 v[56:59], v[168:171], v[214:217], v[56:59]
	v_mfma_f32_16x16x32_bf16 v[52:55], v[176:179], v[214:217], v[52:55]
	s_waitcnt vmcnt(9)
	v_cvt_pk_bf16_f32 v244, v88, v89
	v_cvt_pk_bf16_f32 v245, v90, v91
	ds_write_b64 v194, v[244:245] offset:16384
	s_add_u32 s98, s2, 0x8000
	s_addc_u32 s99, s3, 0
	global_load_dwordx4 v[88:91], v189, s[98:99]
	s_waitcnt lgkmcnt(7)
	v_mfma_f32_16x16x32_bf16 v[40:43], v[168:171], v[224:227], v[40:43]
	v_mfma_f32_16x16x32_bf16 v[36:39], v[176:179], v[224:227], v[36:39]
	s_waitcnt vmcnt(9)
	v_cvt_pk_bf16_f32 v244, v84, v85
	v_cvt_pk_bf16_f32 v245, v86, v87
	ds_write_b64 v196, v[244:245]
	s_add_u32 s100, s48, 0x8000
	s_addc_u32 s101, s49, 0
	global_load_dwordx4 v[84:87], v189, s[100:101]
	s_waitcnt lgkmcnt(7)
	v_mfma_f32_16x16x32_bf16 v[24:27], v[168:171], v[232:235], v[24:27]
	v_mfma_f32_16x16x32_bf16 v[20:23], v[176:179], v[232:235], v[20:23]
	s_waitcnt vmcnt(9)
	v_cvt_pk_bf16_f32 v244, v96, v97
	v_cvt_pk_bf16_f32 v245, v98, v99
	ds_write_b64 v194, v[244:245]
	s_add_u32 s98, s2, 0xc000
	s_addc_u32 s99, s3, 0
	global_load_dwordx4 v[96:99], v189, s[98:99]
	s_waitcnt lgkmcnt(7)
	v_mfma_f32_16x16x32_bf16 v[8:11], v[168:171], v[240:243], v[8:11]
	v_mfma_f32_16x16x32_bf16 v[4:7], v[176:179], v[240:243], v[2:5]
	s_waitcnt vmcnt(9)
	v_cvt_pk_bf16_f32 v244, v92, v93
	v_cvt_pk_bf16_f32 v245, v94, v95
	ds_write_b64 v195, v[244:245]
	s_add_u32 s100, s48, 0xc000
	s_addc_u32 s101, s49, 0
	global_load_dwordx4 v[92:95], v189, s[100:101]
	s_setprio 0
.LBB0_868:
.Lswp_dnO_tail:
	s_add_i32 m0, s21, 0x8000
	s_waitcnt vmcnt(8)
	s_waitcnt lgkmcnt(0)
	s_barrier
	s_cmp_gt_u32 s34, 13
	s_cbranch_scc1 .LBB0_870
	global_load_lds_dwordx4 v[250:251], off
	s_add_i32 m0, s21, 0xa000
	s_mov_b32 s35, s34
	global_load_lds_dwordx4 v[252:253], off
	s_andn2_b64 vcc, exec, s[0:1]
	s_add_i32 m0, s21, 0xc000
	s_cbranch_vccnz .Lrot_dn_two
	global_load_lds_dwordx4 v[222:223], off
	s_add_i32 m0, s21, 0xe000
	s_nop 0
	global_load_lds_dwordx4 v[246:247], off
.Lrot_dn_two:
	s_add_i32 s34, s35, 2
	s_mov_b32 s48, s34
	s_ashr_i32 s49, s48, 31
	s_mov_b64 s[50:51], s[94:95]
	v_cndmask_b32_e64 v1, 0, 1, s[0:1]
	v_cmp_ne_u32_e64 s[2:3], 1, v1
	s_branch .LBB0_858

.Lswp_dnO_half:
	ds_read_b64_tr_b16 v[164:165], v190 offset:32768
	ds_read_b64_tr_b16 v[166:167], v191 offset:32768
	ds_read_b64_tr_b16 v[172:173], v192 offset:32768
	ds_read_b64_tr_b16 v[174:175], v193 offset:32768
	ds_read_b128 v[210:213], v207 offset:32768
	ds_read_b128 v[218:221], v207 offset:34816
	ds_read_b128 v[228:231], v207 offset:36864
	ds_read_b128 v[236:239], v207 offset:38912
	ds_read_b64_tr_b16 v[168:169], v190 offset:40960
	ds_read_b64_tr_b16 v[170:171], v191 offset:40960
	ds_read_b64_tr_b16 v[176:177], v192 offset:40960
	ds_read_b64_tr_b16 v[178:179], v193 offset:40960
	ds_read_b128 v[214:217], v207 offset:33792
	ds_read_b128 v[224:227], v207 offset:35840
	ds_read_b128 v[232:235], v207 offset:37888
	ds_read_b128 v[240:243], v207 offset:39936
	s_lshl_b64 s[2:3], s[48:49], 19
	s_add_u32 s48, s2, 0x80000
	s_addc_u32 s49, s3, 0
	s_add_u32 s2, s74, s48
	s_addc_u32 s3, s43, s49
	s_add_u32 s48, s37, s48
	s_addc_u32 s49, s35, s49
	s_add_i32 s94, s34, 2
	s_ashr_i32 s95, s94, 31
	s_lshl_b64 s[94:95], s[94:95], 7
	s_add_u32 s94, s22, s94
	s_addc_u32 s95, s23, s95
	s_add_u32 s94, s94, 0x80
	s_addc_u32 s95, s95, 0
	v_lshl_add_u64 v[250:251], s[94:95], 0, v[180:181]
	v_lshl_add_u64 v[252:253], s[94:95], 0, v[182:183]
	v_lshl_add_u64 v[222:223], s[94:95], 0, v[184:185]
	v_lshl_add_u64 v[246:247], s[94:95], 0, v[186:187]
	s_setprio 1
	s_waitcnt lgkmcnt(11)
	v_mfma_f32_16x16x32_bf16 v[160:163], v[164:167], v[210:213], v[160:163]
	v_mfma_f32_16x16x32_bf16 v[156:159], v[172:175], v[210:213], v[156:159]
	ds_read_b128 v[210:213], v207 offset:32768
	s_waitcnt lgkmcnt(11)
	v_mfma_f32_16x16x32_bf16 v[152:155], v[164:167], v[218:221], v[152:155]
	v_mfma_f32_16x16x32_bf16 v[148:151], v[172:175], v[218:221], v[148:151]
	ds_read_b128 v[218:221], v207 offset:34816
	s_waitcnt lgkmcnt(11)
	v_mfma_f32_16x16x32_bf16 v[136:139], v[164:167], v[228:231], v[136:139]
	v_mfma_f32_16x16x32_bf16 v[132:135], v[172:175], v[228:231], v[132:135]
	ds_read_b128 v[228:231], v207 offset:36864
	s_waitcnt lgkmcnt(11)
	v_mfma_f32_16x16x32_bf16 v[120:123], v[164:167], v[236:239], v[120:123]
	v_mfma_f32_16x16x32_bf16 v[116:119], v[172:175], v[236:239], v[116:119]
	ds_read_b128 v[236:239], v207 offset:38912
	ds_read_b64_tr_b16 v[164:165], v190 offset:49152
	ds_read_b64_tr_b16 v[166:167], v191 offset:49152
	ds_read_b64_tr_b16 v[172:173], v192 offset:49152
	ds_read_b64_tr_b16 v[174:175], v193 offset:49152
	s_waitcnt lgkmcnt(11)
	v_mfma_f32_16x16x32_bf16 v[160:163], v[168:171], v[214:217], v[160:163]
	v_mfma_f32_16x16x32_bf16 v[156:159], v[176:179], v[214:217], v[156:159]
	ds_read_b128 v[214:217], v207 offset:33792
	s_waitcnt lgkmcnt(11)
	v_mfma_f32_16x16x32_bf16 v[152:155], v[168:171], v[224:227], v[152:155]
	v_mfma_f32_16x16x32_bf16 v[148:151], v[176:179], v[224:227], v[148:151]
	ds_read_b128 v[224:227], v207 offset:35840
	s_waitcnt lgkmcnt(11)
	v_mfma_f32_16x16x32_bf16 v[136:139], v[168:171], v[232:235], v[136:139]
	v_mfma_f32_16x16x32_bf16 v[132:135], v[176:179], v[232:235], v[132:135]
	ds_read_b128 v[232:235], v207 offset:37888
	s_waitcnt lgkmcnt(11)
	v_mfma_f32_16x16x32_bf16 v[120:123], v[168:171], v[240:243], v[120:123]
	v_mfma_f32_16x16x32_bf16 v[116:119], v[176:179], v[240:243], v[116:119]
	ds_read_b128 v[240:243], v207 offset:39936
	ds_read_b64_tr_b16 v[168:169], v190 offset:57344
	ds_read_b64_tr_b16 v[170:171], v191 offset:57344
	ds_read_b64_tr_b16 v[176:177], v192 offset:57344
	ds_read_b64_tr_b16 v[178:179], v193 offset:57344
	s_waitcnt lgkmcnt(8)
	v_mfma_f32_16x16x32_bf16 v[144:147], v[164:167], v[210:213], v[144:147]
	v_mfma_f32_16x16x32_bf16 v[140:143], v[172:175], v[210:213], v[140:143]
	s_waitcnt vmcnt(9)
	v_cvt_pk_bf16_f32 v244, v64, v65
	v_cvt_pk_bf16_f32 v245, v66, v67
	ds_write_b64 v196, v[244:245] offset:16384
	global_load_dwordx4 v[64:67], v189, s[2:3]
	v_mfma_f32_16x16x32_bf16 v[128:131], v[164:167], v[218:221], v[128:131]
	v_mfma_f32_16x16x32_bf16 v[124:127], v[172:175], v[218:221], v[124:127]
	s_waitcnt vmcnt(9)
	v_cvt_pk_bf16_f32 v244, v60, v61
	v_cvt_pk_bf16_f32 v245, v62, v63
	ds_write_b64 v197, v[244:245] offset:16384
	global_load_dwordx4 v[60:63], v189, s[48:49]
	v_mfma_f32_16x16x32_bf16 v[112:115], v[164:167], v[228:231], v[112:115]
	v_mfma_f32_16x16x32_bf16 v[108:111], v[172:175], v[228:231], v[108:111]
	s_waitcnt vmcnt(9)
	v_cvt_pk_bf16_f32 v244, v76, v77
	v_cvt_pk_bf16_f32 v245, v78, v79
	ds_write_b64 v195, v[244:245] offset:16384
	s_add_u32 s98, s2, 0x4000
	s_addc_u32 s99, s3, 0
	global_load_dwordx4 v[76:79], v189, s[98:99]
	v_mfma_f32_16x16x32_bf16 v[104:107], v[164:167], v[236:239], v[104:107]
	v_mfma_f32_16x16x32_bf16 v[100:103], v[172:175], v[236:239], v[100:103]
	s_waitcnt vmcnt(9)
	v_cvt_pk_bf16_f32 v244, v72, v73
	v_cvt_pk_bf16_f32 v245, v74, v75
	ds_write_b64 v197, v[244:245]
	s_add_u32 s100, s48, 0x4000
	s_addc_u32 s101, s49, 0
	global_load_dwordx4 v[72:75], v189, s[100:101]
	s_waitcnt lgkmcnt(4)
	v_mfma_f32_16x16x32_bf16 v[144:147], v[168:171], v[214:217], v[144:147]
	v_mfma_f32_16x16x32_bf16 v[140:143], v[176:179], v[214:217], v[140:143]
	s_waitcnt vmcnt(9)
	v_cvt_pk_bf16_f32 v244, v88, v89
	v_cvt_pk_bf16_f32 v245, v90, v91
	ds_write_b64 v194, v[244:245] offset:16384
	s_add_u32 s98, s2, 0x8000
	s_addc_u32 s99, s3, 0
	global_load_dwordx4 v[88:91], v189, s[98:99]
	v_mfma_f32_16x16x32_bf16 v[128:131], v[168:171], v[224:227], v[128:131]
	v_mfma_f32_16x16x32_bf16 v[124:127], v[176:179], v[224:227], v[124:127]
	s_waitcnt vmcnt(9)
	v_cvt_pk_bf16_f32 v244, v84, v85
	v_cvt_pk_bf16_f32 v245, v86, v87
	ds_write_b64 v196, v[244:245]
	s_add_u32 s100, s48, 0x8000
	s_addc_u32 s101, s49, 0
	global_load_dwordx4 v[84:87], v189, s[100:101]
	v_mfma_f32_16x16x32_bf16 v[112:115], v[168:171], v[232:235], v[112:115]
	v_mfma_f32_16x16x32_bf16 v[108:111], v[176:179], v[232:235], v[108:111]
	s_waitcnt vmcnt(9)
	v_cvt_pk_bf16_f32 v244, v96, v97
	v_cvt_pk_bf16_f32 v245, v98, v99
	ds_write_b64 v194, v[244:245]
	s_add_u32 s98, s2, 0xc000
	s_addc_u32 s99, s3, 0
	global_load_dwordx4 v[96:99], v189, s[98:99]
	v_mfma_f32_16x16x32_bf16 v[104:107], v[168:171], v[240:243], v[104:107]
	v_mfma_f32_16x16x32_bf16 v[100:103], v[176:179], v[240:243], v[100:103]
	s_waitcnt vmcnt(9)
	v_cvt_pk_bf16_f32 v244, v92, v93
	v_cvt_pk_bf16_f32 v245, v94, v95
	ds_write_b64 v195, v[244:245]
	s_add_u32 s100, s48, 0xc000
	s_addc_u32 s101, s49, 0
	global_load_dwordx4 v[92:95], v189, s[100:101]
	s_setprio 0
	s_branch .Lswp_dnO_tail
